# XCD leader's L2/L1 invalidate only at every second (odd) barrier, the parity rule the non-leaders' L1 invalidate already uses
# speedup vs baseline: 1.0005x; 1.0005x over previous
.LBB0_225:
	v_readlane_b32 s3, v249, 34
	s_lshl_b32 s3, s3, 8
	s_waitcnt vmcnt(0)
	v_mov_b32_e32 v2, 0x24808
	ds_read_b32 v2, v2
	s_waitcnt lgkmcnt(0)
	v_and_b32_e32 v2, 1, v2
	v_cmp_eq_u32_e32 vcc, 0, v2
	s_cbranch_vccnz .Lskipinv_0
	buffer_inv sc1
	s_waitcnt vmcnt(0)
.Lskipinv_0:
	s_add_u32 s3, s94, s3
	s_addc_u32 s7, s95, 0
	s_add_u32 s6, s3, 0x2400
	s_addc_u32 s7, s7, 0
	s_mov_b64 s[10:11], -1
	s_mov_b64 s[8:9], exec
	v_mbcnt_lo_u32_b32 v0, s8, 0
	v_mbcnt_hi_u32_b32 v0, s9, v0
	v_cmp_eq_u32_e32 vcc, 0, v0
	s_and_b64 s[10:11], exec, vcc
	s_mov_b64 exec, s[10:11]
	s_cbranch_execz .LBB0_239
	s_bcnt1_i32_b64 s3, s[8:9]
	v_mov_b32_e32 v0, 0
	v_mov_b32_e32 v1, s3
	global_atomic_add v0, v1, s[6:7]
	s_branch .LBB0_239

.Lskipinv_2:
	s_add_u32 s3, s94, s3
	s_addc_u32 s5, s95, 0
	s_add_u32 s4, s3, 0x2400
	s_addc_u32 s5, s5, 0
	s_mov_b64 s[10:11], -1
	s_mov_b64 s[8:9], exec
	v_mbcnt_lo_u32_b32 v0, s8, 0
	v_mbcnt_hi_u32_b32 v0, s9, v0
	v_cmp_eq_u32_e32 vcc, 0, v0
	s_and_b64 s[10:11], exec, vcc
	s_mov_b64 exec, s[10:11]
	s_cbranch_execz .LBB0_710
	s_bcnt1_i32_b64 s3, s[8:9]
	v_mov_b32_e32 v0, 0
	v_mov_b32_e32 v1, s3
	global_atomic_add v0, v1, s[4:5]
	s_branch .LBB0_710

.Lskipinv_4:
	s_add_u32 s3, s94, s3
	s_addc_u32 s13, s95, 0
	s_add_u32 s12, s3, 0x2400
	s_addc_u32 s13, s13, 0
	s_mov_b64 s[16:17], -1
	s_mov_b64 s[14:15], exec
	v_mbcnt_lo_u32_b32 v0, s14, 0
	v_mbcnt_hi_u32_b32 v0, s15, v0
	v_cmp_eq_u32_e32 vcc, 0, v0
	s_and_b64 s[16:17], exec, vcc
	s_mov_b64 exec, s[16:17]
	s_cbranch_execz .LBB0_1074
	s_bcnt1_i32_b64 s3, s[14:15]
	v_mov_b32_e32 v0, 0
	v_mov_b32_e32 v1, s3
	global_atomic_add v0, v1, s[12:13]
	s_branch .LBB0_1074

.Lskipinv_5:
	s_add_u32 s3, s94, s3
	s_addc_u32 s7, s95, 0
	s_add_u32 s6, s3, 0x2400
	s_addc_u32 s7, s7, 0
	s_mov_b64 s[12:13], -1
	s_mov_b64 s[10:11], exec
	v_mbcnt_lo_u32_b32 v0, s10, 0
	v_mbcnt_hi_u32_b32 v0, s11, v0
	v_cmp_eq_u32_e32 vcc, 0, v0
	s_and_b64 s[12:13], exec, vcc
	s_mov_b64 exec, s[12:13]
	s_cbranch_execz .LBB0_1589
	s_bcnt1_i32_b64 s3, s[10:11]
	v_mov_b32_e32 v0, 0
	v_mov_b32_e32 v1, s3
	global_atomic_add v0, v1, s[6:7]
	s_branch .LBB0_1589

.Lskipinv_8:
	s_add_u32 s3, s94, s3
	s_addc_u32 s5, s95, 0
	s_add_u32 s4, s3, 0x2400
	s_addc_u32 s5, s5, 0
	s_mov_b64 s[12:13], -1
	s_mov_b64 s[10:11], exec
	v_mbcnt_lo_u32_b32 v0, s10, 0
	v_mbcnt_hi_u32_b32 v0, s11, v0
	v_cmp_eq_u32_e32 vcc, 0, v0
	s_and_b64 s[12:13], exec, vcc
	s_mov_b64 exec, s[12:13]
	s_cbranch_execz .LBB0_2122
	s_bcnt1_i32_b64 s3, s[10:11]
	v_mov_b32_e32 v0, 0
	v_mov_b32_e32 v1, s3
	global_atomic_add v0, v1, s[4:5]
	s_branch .LBB0_2122

.Lskipinv_9:
	s_add_u32 s3, s94, s3
	s_addc_u32 s7, s95, 0
	s_add_u32 s6, s3, 0x2400
	s_addc_u32 s7, s7, 0
	s_mov_b64 s[14:15], -1
	s_mov_b64 s[10:11], exec
	v_mbcnt_lo_u32_b32 v0, s10, 0
	v_mbcnt_hi_u32_b32 v0, s11, v0
	v_cmp_eq_u32_e32 vcc, 0, v0
	s_and_b64 s[14:15], exec, vcc
	s_mov_b64 exec, s[14:15]
	s_cbranch_execz .LBB0_2301
	s_bcnt1_i32_b64 s3, s[10:11]
	v_mov_b32_e32 v0, 0
	v_mov_b32_e32 v1, s3
	global_atomic_add v0, v1, s[6:7]
	s_branch .LBB0_2301

.LBB0_2911:
	v_readlane_b32 s2, v249, 34
	s_lshl_b32 s2, s2, 8
	s_waitcnt vmcnt(0)
	v_mov_b32_e32 v2, 0x24808
	ds_read_b32 v2, v2
	s_waitcnt lgkmcnt(0)
	v_and_b32_e32 v2, 1, v2
	v_cmp_eq_u32_e32 vcc, 0, v2
	s_cbranch_vccnz .Lskipinv_12
	buffer_inv sc1
	s_waitcnt vmcnt(0)
.Lskipinv_12:
	s_add_u32 s2, s94, s2
	s_addc_u32 s3, s95, 0
	s_add_u32 s2, s2, 0x2400
	s_addc_u32 s3, s3, 0
	s_mov_b64 s[6:7], -1
	s_mov_b64 s[4:5], exec
	v_mbcnt_lo_u32_b32 v0, s4, 0
	v_mbcnt_hi_u32_b32 v0, s5, v0
	v_cmp_eq_u32_e32 vcc, 0, v0
	s_and_b64 s[6:7], exec, vcc
	s_mov_b64 exec, s[6:7]
	s_cbranch_execz .LBB0_2925
	s_bcnt1_i32_b64 s4, s[4:5]
	v_mov_b32_e32 v0, 0
	v_mov_b32_e32 v1, s4
	global_atomic_add v0, v1, s[2:3]
	s_branch .LBB0_2925
